# MoE phases 8/9: XCD-aware unit order so the WGs sharing an expert's rows sit on one XCD (assumes round-robin WG->XCD)
# speedup vs baseline: 1.0260x; 1.0260x over previous
.LBB0_1004:
	s_or_b64 exec, exec, s[6:7]
	s_add_i32 s3, 0, 0x20100
	v_mov_b32_e32 v0, s3
	s_waitcnt lgkmcnt(0)
	s_barrier
	ds_read_b32 v0, v0
	s_waitcnt lgkmcnt(0)
	v_readfirstlane_b32 s3, v0
	s_lshl_b32 s3, s3, 3
	s_cmp_ge_i32 s2, s3
	s_cbranch_scc1 .LBB0_1025
	s_add_u32 s6, s76, 0x33d78000
	s_addc_u32 s7, s77, 0
	s_add_u32 s8, s76, 0x33f78000
	s_addc_u32 s9, s77, 0
	s_ashr_i32 s14, s10, 6
	s_ashr_i32 s10, s10, 5
	v_bfe_u32 v0, v2, 3, 3
	v_and_or_b32 v6, s10, -8, v0
	s_lshl_b32 s10, s14, 3
	s_and_b32 s10, s10, 24
	s_lshl_b32 s15, s14, 5
	v_and_or_b32 v4, v2, 7, s10
	s_cmp_lt_u32 s10, 16
	s_movk_i32 s10, 0xb0
	s_cselect_b32 s10, s10, 0xb8
	s_add_u32 s12, s0, s10
	v_lshrrev_b32_e32 v0, 2, v6
	s_addc_u32 s13, s1, 0
	s_lshl_b32 s10, s14, 10
	v_bitop3_b32 v0, v0, v2, 3 bitop3:0x78
	v_lshlrev_b32_e32 v1, 8, v4
	s_add_i32 s38, s15, 0x100
	s_add_i32 s39, s10, 0
	v_and_b32_e32 v3, 31, v2
	v_lshl_add_u32 v0, v0, 4, v1
	v_bfe_u32 v1, v2, 1, 5
	s_add_u32 s14, s76, 0x38318000
	v_and_or_b32 v10, v1, 12, v0
	v_or_b32_e32 v0, s15, v1
	v_or_b32_e32 v166, s15, v3
	s_addc_u32 s15, s77, 0
	s_add_u32 s16, s76, 0x38318020
	v_lshlrev_b32_e32 v6, 1, v6
	s_load_dwordx2 s[12:13], s[12:13], 0x0
	s_addc_u32 s17, s77, 0
	v_bfe_u32 v5, v2, 5, 1
	v_lshrrev_b32_e32 v8, 2, v2
	v_ashrrev_i32_e32 v7, 31, v6
	s_add_u32 s18, s76, 0x38318040
	v_bfe_u32 v9, v2, 2, 2
	v_lshlrev_b32_e32 v1, 4, v2
	v_lshlrev_b32_e32 v4, 2, v4
	v_lshlrev_b64 v[148:149], 11, v[6:7]
	v_bitop3_b32 v6, v5, v8, 3 bitop3:0x78
	s_addc_u32 s19, s77, 0
	v_bitop3_b32 v1, v1, 16, v2 bitop3:0x48
	v_and_b32_e32 v4, 60, v4
	v_mov_b32_e32 v147, 0
	v_lshlrev_b32_e32 v162, 4, v6
	v_lshlrev_b32_e32 v2, 1, v2
	v_lshlrev_b32_e32 v6, 3, v5
	v_bitop3_b32 v7, v5, v9, 2 bitop3:0x36
	s_add_u32 s20, s76, 0x39318000
	s_mov_b32 s11, 0
	v_lshlrev_b32_e32 v160, 5, v3
	v_lshl_add_u32 v161, v3, 6, 0
	v_and_or_b32 v163, v2, 16, v6
	v_lshlrev_b32_e32 v164, 4, v7
	v_bitop3_b32 v165, v6, 16, v2 bitop3:0x34
	v_lshlrev_b32_e32 v150, 4, v5
	v_mov_b32_e32 v151, v147
	v_add_u32_e32 v167, 0x100, v0
	v_add_u32_e32 v168, 0x100, v166
	s_addc_u32 s21, s77, 0
	v_lshlrev_b32_e32 v152, 2, v4
	v_mov_b32_e32 v153, v147
	s_mov_b64 s[22:23], 0x800
	s_mov_b64 s[24:25], 0x10000
	s_mov_b64 s[26:27], 0x10800
	s_add_i32 s40, s39, 0x4000
	v_add_u32_e32 v169, 0, v10
	s_mov_b64 s[28:29], 0x20000
	s_mov_b64 s[30:31], 0x20800
	s_add_i32 s41, s39, 0x8000
	s_add_i32 s42, s39, 0x2000
	s_add_i32 s43, s39, 0x6000
	s_add_i32 s44, s39, 0xa000
	v_mov_b32_e32 v155, 0x41800000
	s_mov_b32 s45, 0xc3e00000
	v_mov_b32_e32 v170, 0x43e00000
	s_and_b32 s46, s2, 7
	s_lshl_b32 s46, s46, 5
	s_lshr_b32 s98, s2, 3
	s_or_b32 s46, s46, s98
	s_branch .LBB0_1007

.LBB0_1080:
	s_or_b64 exec, exec, s[6:7]
	s_add_i32 s3, 0, 0x20100
	v_mov_b32_e32 v0, s3
	s_waitcnt lgkmcnt(0)
	s_barrier
	ds_read_b32 v0, v0
	s_waitcnt lgkmcnt(0)
	v_readfirstlane_b32 s3, v0
	s_lshl_b32 s3, s3, 4
	s_cmp_ge_i32 s2, s3
	s_cbranch_scc1 .LBB0_1097
	s_add_u32 s8, s76, 0x33d78000
	s_addc_u32 s9, s77, 0
	s_ashr_i32 s11, s10, 6
	s_ashr_i32 s10, s10, 5
	v_bfe_u32 v0, v2, 3, 3
	v_and_or_b32 v6, s10, -8, v0
	s_lshl_b32 s10, s11, 3
	v_and_b32_e32 v1, 7, v2
	v_and_or_b32 v4, s10, 24, v1
	s_lshl_b32 s10, s11, 5
	s_lshl_b32 s12, s11, 10
	s_add_i32 s38, s10, 0x100
	s_add_i32 s39, s12, 0
	s_add_u32 s12, s76, 0x39318000
	s_addc_u32 s13, s77, 0
	v_lshrrev_b32_e32 v0, 2, v6
	s_add_u32 s14, s76, 0x39318020
	s_load_dwordx2 s[6:7], s[0:1], 0xc0
	v_bitop3_b32 v0, v0, v2, 3 bitop3:0x78
	v_lshlrev_b32_e32 v1, 8, v4
	v_lshlrev_b32_e32 v6, 1, v6
	s_addc_u32 s15, s77, 0
	v_bfe_u32 v5, v2, 5, 1
	v_lshrrev_b32_e32 v8, 2, v2
	v_lshl_add_u32 v0, v0, 4, v1
	v_bfe_u32 v1, v2, 1, 5
	v_ashrrev_i32_e32 v7, 31, v6
	s_add_u32 s16, s76, 0x39318040
	v_and_b32_e32 v3, 31, v2
	v_bfe_u32 v9, v2, 2, 2
	v_and_or_b32 v10, v1, 12, v0
	v_or_b32_e32 v0, s10, v1
	v_lshlrev_b32_e32 v1, 4, v2
	v_lshlrev_b64 v[148:149], 13, v[6:7]
	v_bitop3_b32 v6, v5, v8, 3 bitop3:0x78
	s_addc_u32 s17, s77, 0
	v_bitop3_b32 v1, v1, 16, v2 bitop3:0x48
	v_lshlrev_b32_e32 v4, 2, v4
	v_mov_b32_e32 v147, 0
	v_lshlrev_b32_e32 v160, 4, v6
	v_lshlrev_b32_e32 v2, 1, v2
	v_lshlrev_b32_e32 v6, 3, v5
	v_bitop3_b32 v7, v5, v9, 2 bitop3:0x36
	v_or_b32_e32 v164, s10, v3
	s_add_u32 s18, s76, 0x2dd78000
	s_mov_b32 s11, 0
	v_lshlrev_b32_e32 v158, 5, v3
	v_lshl_add_u32 v159, v3, 6, 0
	v_and_or_b32 v161, v2, 16, v6
	v_lshlrev_b32_e32 v162, 4, v7
	v_bitop3_b32 v163, v6, 16, v2 bitop3:0x34
	v_lshlrev_b32_e32 v150, 4, v5
	v_mov_b32_e32 v151, v147
	v_add_u32_e32 v165, 0x100, v0
	v_add_u32_e32 v166, 0x100, v164
	s_addc_u32 s19, s77, 0
	v_lshlrev_b32_e32 v152, 2, v4
	v_mov_b32_e32 v153, v147
	s_mov_b64 s[20:21], 0x2000
	s_mov_b64 s[22:23], 0x40000
	s_mov_b64 s[24:25], 0x42000
	s_add_i32 s40, s39, 0x4000
	v_add_u32_e32 v167, 0, v10
	s_mov_b64 s[26:27], 0x80000
	s_mov_b64 s[28:29], 0x82000
	s_add_i32 s41, s39, 0x8000
	s_add_i32 s42, s39, 0x2000
	s_add_i32 s43, s39, 0x6000
	s_add_i32 s44, s39, 0xa000
	s_mov_b32 s45, 0xc3e00000
	v_mov_b32_e32 v168, 0x43e00000
	s_and_b32 s46, s2, 7
	s_lshl_b32 s46, s46, 5
	s_lshr_b32 s98, s2, 3
	s_or_b32 s46, s46, s98
	s_branch .LBB0_1083

	.amdhsa_kernel _Z6mk_fwd6Params
		.amdhsa_group_segment_fixed_size 0
		.amdhsa_private_segment_fixed_size 0
		.amdhsa_kernarg_size 1208
		.amdhsa_user_sgpr_count 2
		.amdhsa_user_sgpr_dispatch_ptr 0
		.amdhsa_user_sgpr_queue_ptr 0
		.amdhsa_user_sgpr_kernarg_segment_ptr 1
		.amdhsa_user_sgpr_dispatch_id 0
		.amdhsa_user_sgpr_kernarg_preload_length 0
		.amdhsa_user_sgpr_kernarg_preload_offset 0
		.amdhsa_user_sgpr_private_segment_size 0
		.amdhsa_uses_dynamic_stack 0
		.amdhsa_enable_private_segment 0
		.amdhsa_system_sgpr_workgroup_id_x 1
		.amdhsa_system_sgpr_workgroup_id_y 0
		.amdhsa_system_sgpr_workgroup_id_z 0
		.amdhsa_system_sgpr_workgroup_info 0
		.amdhsa_system_vgpr_workitem_id 0
		.amdhsa_next_free_vgpr 256
		.amdhsa_next_free_sgpr 102
		.amdhsa_accum_offset 256
		.amdhsa_reserve_vcc 1
		.amdhsa_float_round_mode_32 0
		.amdhsa_float_round_mode_16_64 0
		.amdhsa_float_denorm_mode_32 3
		.amdhsa_float_denorm_mode_16_64 3
		.amdhsa_dx10_clamp 1
		.amdhsa_ieee_mode 1
		.amdhsa_fp16_overflow 0
		.amdhsa_tg_split 0
		.amdhsa_exception_fp_ieee_invalid_op 0
		.amdhsa_exception_fp_denorm_src 0
		.amdhsa_exception_fp_ieee_div_zero 0
		.amdhsa_exception_fp_ieee_overflow 0
		.amdhsa_exception_fp_ieee_underflow 0
		.amdhsa_exception_fp_ieee_inexact 0
		.amdhsa_exception_int_div_zero 0
	.end_amdhsa_kernel

amdhsa.kernels:
  - .agpr_count:     0
    .args:
      - .offset:         0
        .size:           952
        .value_kind:     by_value
      - .offset:         952
        .size:           4
        .value_kind:     hidden_block_count_x
      - .offset:         956
        .size:           4
        .value_kind:     hidden_block_count_y
      - .offset:         960
        .size:           4
        .value_kind:     hidden_block_count_z
      - .offset:         964
        .size:           2
        .value_kind:     hidden_group_size_x
      - .offset:         966
        .size:           2
        .value_kind:     hidden_group_size_y
      - .offset:         968
        .size:           2
        .value_kind:     hidden_group_size_z
      - .offset:         970
        .size:           2
        .value_kind:     hidden_remainder_x
      - .offset:         972
        .size:           2
        .value_kind:     hidden_remainder_y
      - .offset:         974
        .size:           2
        .value_kind:     hidden_remainder_z
      - .offset:         992
        .size:           8
        .value_kind:     hidden_global_offset_x
      - .offset:         1000
        .size:           8
        .value_kind:     hidden_global_offset_y
      - .offset:         1008
        .size:           8
        .value_kind:     hidden_global_offset_z
      - .offset:         1016
        .size:           2
        .value_kind:     hidden_grid_dims
      - .offset:         1072
        .size:           4
        .value_kind:     hidden_dynamic_lds_size
    .group_segment_fixed_size: 0
    .kernarg_segment_align: 8
    .kernarg_segment_size: 1208
    .language:       OpenCL C
    .language_version:
      - 2
      - 0
    .max_flat_workgroup_size: 512
    .name:           _Z6mk_fwd6Params
    .private_segment_fixed_size: 0
    .sgpr_count:     108
    .sgpr_spill_count: 5
    .symbol:         _Z6mk_fwd6Params.kd
    .uniform_work_group_size: 1
    .uses_dynamic_stack: false
    .vgpr_count:     256
    .vgpr_spill_count: 0
    .wavefront_size: 64
